# P15: defer gather-index wait to K-loop; peel first K-iteration with C=0 MFMAs (no accumulator zeroing)
# speedup vs baseline: 1.0108x; 1.0108x over previous
.LBB0_1910:
	v_add_u32_e32 v6, s62, v171
	v_add_u32_e32 v2, v6, v192
	v_ashrrev_i32_e32 v3, 31, v2
	v_add_u32_e32 v6, v6, v193
	v_lshl_add_u64 v[4:5], v[2:3], 2, s[10:11]
	v_add_u32_e32 v2, 0x80, v2
	v_ashrrev_i32_e32 v7, 31, v6
	v_ashrrev_i32_e32 v3, 31, v2
	v_lshl_add_u64 v[8:9], v[6:7], 2, s[10:11]
	v_add_u32_e32 v6, 0x80, v6
	v_lshl_add_u64 v[2:3], v[2:3], 2, s[10:11]
	v_ashrrev_i32_e32 v7, 31, v6
	v_lshl_add_u64 v[6:7], v[6:7], 2, s[10:11]
	global_load_dword v236, v[4:5], off
	s_nop 0
	global_load_dword v237, v[2:3], off
	s_nop 0
	global_load_dword v238, v[8:9], off
	global_load_dword v239, v[6:7], off
	v_mov_b32_e32 v175, v169
	v_mov_b32_e32 v179, v169
	s_add_u32 s37, s42, 0x100
	s_mov_b32 s79, -2
	s_mov_b64 s[46:47], 0
	s_addc_u32 s80, s43, 0
	v_lshl_add_u64 v[180:181], s[18:19], 0, v[174:175]
	v_lshl_add_u64 v[182:183], s[18:19], 0, v[178:179]
	ds_read_b128 v[18:21], v197
	ds_read_b128 v[22:25], v197 offset:1024
	ds_read_b128 v[26:29], v197 offset:2048
	ds_read_b128 v[30:33], v197 offset:3072
	ds_read_b128 v[2:5], v198
	ds_read_b128 v[6:9], v198 offset:1024
	ds_read_b128 v[10:13], v198 offset:2048
	ds_read_b128 v[14:17], v198 offset:3072
	s_add_u32 s42, s46, 0x100
	s_addc_u32 s43, s47, 0
	s_add_u32 s48, s37, s46
	s_addc_u32 s49, s80, s47
	s_cmpk_eq_i32 s46, 0x300
	s_cselect_b64 vcc, -1, 0
	s_and_b64 s[44:45], vcc, exec
	s_cselect_b32 s81, 0, s42
	s_cselect_b32 s76, 0, s43
	s_cselect_b32 s44, s38, s48
	s_cselect_b32 s45, s39, s49
	s_add_u32 s48, s8, s81
	s_addc_u32 s49, s9, s76
	v_lshl_add_u64 v[228:229], v[180:181], 0, s[46:47]
	s_add_i32 m0, s41, 0xc000
	ds_read_b128 v[184:187], v199
	ds_read_b128 v[188:191], v199 offset:1024
	ds_read_b128 v[204:207], v199 offset:2048
	ds_read_b128 v[208:211], v199 offset:3072
	ds_read_b128 v[212:215], v199 offset:4096
	ds_read_b128 v[216:219], v199 offset:5120
	ds_read_b128 v[220:223], v199 offset:6144
	ds_read_b128 v[224:227], v199 offset:7168
	global_load_lds_dwordx4 v[228:229], off
	v_lshl_add_u64 v[228:229], v[182:183], 0, s[46:47]
	s_add_i32 m0, s41, 0xe000
	s_nop 0
	global_load_lds_dwordx4 v[228:229], off
	s_waitcnt vmcnt(8)
	s_waitcnt lgkmcnt(0)
	s_barrier
	s_setprio 1
	s_waitcnt lgkmcnt(0)
	v_mfma_scale_f32_16x16x128_f8f6f4 v[158:161], v[18:25], v[184:191], 0, v163, v1 op_sel_hi:[0,0,0]
	v_mfma_scale_f32_16x16x128_f8f6f4 v[150:153], v[26:33], v[184:191], 0, v163, v1 op_sel_hi:[0,0,0]
	v_mfma_scale_f32_16x16x128_f8f6f4 v[142:145], v[18:25], v[204:211], 0, v163, v1 op_sel_hi:[0,0,0]
	v_mfma_scale_f32_16x16x128_f8f6f4 v[134:137], v[26:33], v[204:211], 0, v163, v1 op_sel_hi:[0,0,0]
	v_mfma_scale_f32_16x16x128_f8f6f4 v[126:129], v[18:25], v[212:219], 0, v163, v1 op_sel_hi:[0,0,0]
	v_mfma_scale_f32_16x16x128_f8f6f4 v[118:121], v[26:33], v[212:219], 0, v163, v1 op_sel_hi:[0,0,0]
	v_mfma_scale_f32_16x16x128_f8f6f4 v[110:113], v[18:25], v[220:227], 0, v163, v1 op_sel_hi:[0,0,0]
	v_mfma_scale_f32_16x16x128_f8f6f4 v[102:105], v[26:33], v[220:227], 0, v163, v1 op_sel_hi:[0,0,0]
	s_setprio 0
	s_setprio 1
	v_mfma_scale_f32_16x16x128_f8f6f4 v[154:157], v[2:9], v[184:191], 0, v163, v1 op_sel_hi:[0,0,0]
	v_mfma_scale_f32_16x16x128_f8f6f4 v[146:149], v[10:17], v[184:191], 0, v163, v1 op_sel_hi:[0,0,0]
	v_mfma_scale_f32_16x16x128_f8f6f4 v[138:141], v[2:9], v[204:211], 0, v163, v1 op_sel_hi:[0,0,0]
	v_mfma_scale_f32_16x16x128_f8f6f4 v[130:133], v[10:17], v[204:211], 0, v163, v1 op_sel_hi:[0,0,0]
	v_mfma_scale_f32_16x16x128_f8f6f4 v[122:125], v[2:9], v[212:219], 0, v163, v1 op_sel_hi:[0,0,0]
	v_mfma_scale_f32_16x16x128_f8f6f4 v[114:117], v[10:17], v[212:219], 0, v163, v1 op_sel_hi:[0,0,0]
	v_mfma_scale_f32_16x16x128_f8f6f4 v[106:109], v[2:9], v[220:227], 0, v163, v1 op_sel_hi:[0,0,0]
	v_mfma_scale_f32_16x16x128_f8f6f4 v[98:101], v[10:17], v[220:227], 0, v163, v1 op_sel_hi:[0,0,0]
	s_setprio 0
	s_barrier
	s_add_i32 s46, s5, s52
	v_lshl_add_u64 v[184:185], s[44:45], 0, v[164:165]
	s_mov_b32 m0, s46
	ds_read_b128 v[204:207], v199 offset:16384
	ds_read_b128 v[208:211], v199 offset:17408
	ds_read_b128 v[212:215], v199 offset:18432
	ds_read_b128 v[216:219], v199 offset:19456
	ds_read_b128 v[220:223], v199 offset:20480
	ds_read_b128 v[224:227], v199 offset:21504
	ds_read_b128 v[228:231], v199 offset:22528
	ds_read_b128 v[232:235], v199 offset:23552
	global_load_lds_dwordx4 v[184:185], off
	s_add_i32 m0, s46, 0x2000
	s_add_u32 s46, s44, 0x20000
	v_lshl_add_u64 v[186:187], s[44:45], 0, v[166:167]
	s_addc_u32 s47, s45, 0
	s_add_i32 s76, s66, s52
	global_load_lds_dwordx4 v[186:187], off
	v_lshl_add_u64 v[188:189], s[46:47], 0, v[164:165]
	s_mov_b32 m0, s76
	v_cndmask_b32_e32 v168, v202, v179, vcc
	global_load_lds_dwordx4 v[188:189], off
	v_lshl_add_u64 v[188:189], s[46:47], 0, v[166:167]
	s_add_i32 m0, s76, 0x2000
	v_lshl_add_u64 v[190:191], s[48:49], 0, v[168:169]
	global_load_lds_dwordx4 v[188:189], off
	s_mov_b32 m0, s41
	v_cndmask_b32_e32 v188, v176, v201, vcc
	global_load_lds_dwordx4 v168, s[48:49]
	s_mov_b32 m0, s53
	v_mov_b32_e32 v189, v169
	global_load_lds_dwordx4 v188, s[48:49]
	s_waitcnt vmcnt(8)
	s_waitcnt lgkmcnt(0)
	v_lshl_add_u64 v[188:189], s[48:49], 0, v[188:189]
	s_barrier
	s_setprio 1
	s_waitcnt lgkmcnt(0)
	v_mfma_scale_f32_16x16x128_f8f6f4 v[94:97], v[18:25], v[204:211], 0, v163, v1 op_sel_hi:[0,0,0]
	v_mfma_scale_f32_16x16x128_f8f6f4 v[86:89], v[26:33], v[204:211], 0, v163, v1 op_sel_hi:[0,0,0]
	v_mfma_scale_f32_16x16x128_f8f6f4 v[78:81], v[18:25], v[212:219], 0, v163, v1 op_sel_hi:[0,0,0]
	v_mfma_scale_f32_16x16x128_f8f6f4 v[70:73], v[26:33], v[212:219], 0, v163, v1 op_sel_hi:[0,0,0]
	v_mfma_scale_f32_16x16x128_f8f6f4 v[58:61], v[18:25], v[220:227], 0, v163, v1 op_sel_hi:[0,0,0]
	v_mfma_scale_f32_16x16x128_f8f6f4 v[46:49], v[26:33], v[220:227], 0, v163, v1 op_sel_hi:[0,0,0]
	v_mfma_scale_f32_16x16x128_f8f6f4 v[38:41], v[18:25], v[228:235], 0, v163, v1 op_sel_hi:[0,0,0]
	v_mfma_scale_f32_16x16x128_f8f6f4 v[34:37], v[26:33], v[228:235], 0, v163, v1 op_sel_hi:[0,0,0]
	s_setprio 0
	s_setprio 1
	v_mfma_scale_f32_16x16x128_f8f6f4 v[90:93], v[2:9], v[204:211], 0, v163, v1 op_sel_hi:[0,0,0]
	v_mfma_scale_f32_16x16x128_f8f6f4 v[82:85], v[10:17], v[204:211], 0, v163, v1 op_sel_hi:[0,0,0]
	v_mfma_scale_f32_16x16x128_f8f6f4 v[74:77], v[2:9], v[212:219], 0, v163, v1 op_sel_hi:[0,0,0]
	v_mfma_scale_f32_16x16x128_f8f6f4 v[66:69], v[10:17], v[212:219], 0, v163, v1 op_sel_hi:[0,0,0]
	v_mfma_scale_f32_16x16x128_f8f6f4 v[50:53], v[2:9], v[220:227], 0, v163, v1 op_sel_hi:[0,0,0]
	v_mfma_scale_f32_16x16x128_f8f6f4 v[42:45], v[10:17], v[220:227], 0, v163, v1 op_sel_hi:[0,0,0]
	v_mfma_scale_f32_16x16x128_f8f6f4 v[62:65], v[2:9], v[228:235], 0, v163, v1 op_sel_hi:[0,0,0]
	v_mfma_scale_f32_16x16x128_f8f6f4 v[54:57], v[10:17], v[228:235], 0, v163, v1 op_sel_hi:[0,0,0]
	s_setprio 0
	s_barrier
	s_add_i32 s46, 0, 0x18000
	s_add_i32 s47, 0, 0x1c000
	v_add_u32_e32 v14, s46, v177
	v_add_u32_e32 v30, s47, v177
	ds_read_b128 v[2:5], v14
	ds_read_b128 v[6:9], v14 offset:1024
	ds_read_b128 v[10:13], v14 offset:2048
	ds_read_b128 v[14:17], v14 offset:3072
	ds_read_b128 v[18:21], v30
	ds_read_b128 v[22:25], v30 offset:1024
	ds_read_b128 v[26:29], v30 offset:2048
	ds_read_b128 v[30:33], v30 offset:3072
	s_mov_b32 m0, s59
	v_cndmask_b32_e32 v168, v174, v175, vcc
	ds_read_b128 v[204:207], v199 offset:32768
	ds_read_b128 v[208:211], v199 offset:33792
	ds_read_b128 v[212:215], v199 offset:34816
	ds_read_b128 v[216:219], v199 offset:35840
	ds_read_b128 v[220:223], v199 offset:36864
	ds_read_b128 v[224:227], v199 offset:37888
	ds_read_b128 v[228:231], v199 offset:38912
	ds_read_b128 v[232:235], v199 offset:39936
	v_cndmask_b32_e32 v170, v178, v200, vcc
	global_load_lds_dwordx4 v168, s[48:49]
	s_mov_b32 m0, s60
	s_nop 0
	global_load_lds_dwordx4 v170, s[48:49]
	s_waitcnt vmcnt(8)
	s_waitcnt lgkmcnt(0)
	s_barrier
	s_setprio 1
	s_waitcnt lgkmcnt(0)
	v_mfma_scale_f32_16x16x128_f8f6f4 v[158:161], v[2:9], v[204:211], v[158:161], v163, v1 op_sel_hi:[0,0,0]
	v_mfma_scale_f32_16x16x128_f8f6f4 v[150:153], v[10:17], v[204:211], v[150:153], v163, v1 op_sel_hi:[0,0,0]
	v_mfma_scale_f32_16x16x128_f8f6f4 v[142:145], v[2:9], v[212:219], v[142:145], v163, v1 op_sel_hi:[0,0,0]
	v_mfma_scale_f32_16x16x128_f8f6f4 v[134:137], v[10:17], v[212:219], v[134:137], v163, v1 op_sel_hi:[0,0,0]
	v_mfma_scale_f32_16x16x128_f8f6f4 v[126:129], v[2:9], v[220:227], v[126:129], v163, v1 op_sel_hi:[0,0,0]
	v_mfma_scale_f32_16x16x128_f8f6f4 v[118:121], v[10:17], v[220:227], v[118:121], v163, v1 op_sel_hi:[0,0,0]
	v_mfma_scale_f32_16x16x128_f8f6f4 v[110:113], v[2:9], v[228:235], v[110:113], v163, v1 op_sel_hi:[0,0,0]
	v_mfma_scale_f32_16x16x128_f8f6f4 v[102:105], v[10:17], v[228:235], v[102:105], v163, v1 op_sel_hi:[0,0,0]
	s_setprio 0
	s_setprio 1
	v_mfma_scale_f32_16x16x128_f8f6f4 v[154:157], v[18:25], v[204:211], v[154:157], v163, v1 op_sel_hi:[0,0,0]
	v_mfma_scale_f32_16x16x128_f8f6f4 v[146:149], v[26:33], v[204:211], v[146:149], v163, v1 op_sel_hi:[0,0,0]
	v_mfma_scale_f32_16x16x128_f8f6f4 v[138:141], v[18:25], v[212:219], v[138:141], v163, v1 op_sel_hi:[0,0,0]
	v_mfma_scale_f32_16x16x128_f8f6f4 v[130:133], v[26:33], v[212:219], v[130:133], v163, v1 op_sel_hi:[0,0,0]
	v_mfma_scale_f32_16x16x128_f8f6f4 v[122:125], v[18:25], v[220:227], v[122:125], v163, v1 op_sel_hi:[0,0,0]
	v_mfma_scale_f32_16x16x128_f8f6f4 v[114:117], v[26:33], v[220:227], v[114:117], v163, v1 op_sel_hi:[0,0,0]
	v_mfma_scale_f32_16x16x128_f8f6f4 v[106:109], v[18:25], v[228:235], v[106:109], v163, v1 op_sel_hi:[0,0,0]
	v_mfma_scale_f32_16x16x128_f8f6f4 v[98:101], v[26:33], v[228:235], v[98:101], v163, v1 op_sel_hi:[0,0,0]
	s_setprio 0
	s_barrier
	s_add_i32 s46, s46, s52
	v_lshl_add_u64 v[184:185], v[184:185], 0, s[16:17]
	s_mov_b32 m0, s46
	ds_read_b128 v[204:207], v199 offset:49152
	ds_read_b128 v[208:211], v199 offset:50176
	ds_read_b128 v[212:215], v199 offset:51200
	ds_read_b128 v[216:219], v199 offset:52224
	ds_read_b128 v[220:223], v199 offset:53248
	ds_read_b128 v[224:227], v199 offset:54272
	ds_read_b128 v[228:231], v199 offset:55296
	ds_read_b128 v[232:235], v199 offset:56320
	global_load_lds_dwordx4 v[184:185], off
	s_add_i32 m0, s46, 0x2000
	s_add_u32 s44, s44, 0x20080
	v_lshl_add_u64 v[184:185], v[186:187], 0, s[16:17]
	s_addc_u32 s45, s45, 0
	s_add_i32 s46, s47, s52
	global_load_lds_dwordx4 v[184:185], off
	v_lshl_add_u64 v[184:185], s[44:45], 0, v[164:165]
	s_mov_b32 m0, s46
	s_nop 0
	global_load_lds_dwordx4 v[184:185], off
	v_lshl_add_u64 v[184:185], s[44:45], 0, v[166:167]
	s_add_i32 m0, s46, 0x2000
	s_nop 0
	global_load_lds_dwordx4 v[184:185], off
	v_lshl_add_u64 v[184:185], v[190:191], 0, s[16:17]
	s_mov_b32 m0, s63
	s_nop 0
	global_load_lds_dwordx4 v[184:185], off
	v_lshl_add_u64 v[184:185], v[188:189], 0, s[16:17]
	s_mov_b32 m0, s64
	s_nop 0
	global_load_lds_dwordx4 v[184:185], off
	s_waitcnt vmcnt(8)
	s_waitcnt lgkmcnt(0)
	s_barrier
	s_setprio 1
	s_waitcnt lgkmcnt(0)
	v_mfma_scale_f32_16x16x128_f8f6f4 v[94:97], v[2:9], v[204:211], v[94:97], v163, v1 op_sel_hi:[0,0,0]
	v_mfma_scale_f32_16x16x128_f8f6f4 v[86:89], v[10:17], v[204:211], v[86:89], v163, v1 op_sel_hi:[0,0,0]
	v_mfma_scale_f32_16x16x128_f8f6f4 v[78:81], v[2:9], v[212:219], v[78:81], v163, v1 op_sel_hi:[0,0,0]
	v_mfma_scale_f32_16x16x128_f8f6f4 v[70:73], v[10:17], v[212:219], v[70:73], v163, v1 op_sel_hi:[0,0,0]
	v_mfma_scale_f32_16x16x128_f8f6f4 v[58:61], v[2:9], v[220:227], v[58:61], v163, v1 op_sel_hi:[0,0,0]
	v_mfma_scale_f32_16x16x128_f8f6f4 v[46:49], v[10:17], v[220:227], v[46:49], v163, v1 op_sel_hi:[0,0,0]
	v_mfma_scale_f32_16x16x128_f8f6f4 v[38:41], v[2:9], v[228:235], v[38:41], v163, v1 op_sel_hi:[0,0,0]
	v_mfma_scale_f32_16x16x128_f8f6f4 v[34:37], v[10:17], v[228:235], v[34:37], v163, v1 op_sel_hi:[0,0,0]
	s_setprio 0
	s_setprio 1
	v_mfma_scale_f32_16x16x128_f8f6f4 v[90:93], v[18:25], v[204:211], v[90:93], v163, v1 op_sel_hi:[0,0,0]
	v_mfma_scale_f32_16x16x128_f8f6f4 v[82:85], v[26:33], v[204:211], v[82:85], v163, v1 op_sel_hi:[0,0,0]
	v_mfma_scale_f32_16x16x128_f8f6f4 v[74:77], v[18:25], v[212:219], v[74:77], v163, v1 op_sel_hi:[0,0,0]
	v_mfma_scale_f32_16x16x128_f8f6f4 v[66:69], v[26:33], v[212:219], v[66:69], v163, v1 op_sel_hi:[0,0,0]
	v_mfma_scale_f32_16x16x128_f8f6f4 v[50:53], v[18:25], v[220:227], v[50:53], v163, v1 op_sel_hi:[0,0,0]
	v_mfma_scale_f32_16x16x128_f8f6f4 v[42:45], v[26:33], v[220:227], v[42:45], v163, v1 op_sel_hi:[0,0,0]
	v_mfma_scale_f32_16x16x128_f8f6f4 v[62:65], v[18:25], v[228:235], v[62:65], v163, v1 op_sel_hi:[0,0,0]
	v_mfma_scale_f32_16x16x128_f8f6f4 v[54:57], v[26:33], v[228:235], v[54:57], v163, v1 op_sel_hi:[0,0,0]
	s_setprio 0
	s_barrier
	s_add_i32 s79, s79, 2
	s_cmp_gt_u32 s79, 5
	s_mov_b64 s[46:47], s[42:43]
.LBB0_1911:
	ds_read_b128 v[18:21], v197
	ds_read_b128 v[22:25], v197 offset:1024
	ds_read_b128 v[26:29], v197 offset:2048
	ds_read_b128 v[30:33], v197 offset:3072
	ds_read_b128 v[2:5], v198
	ds_read_b128 v[6:9], v198 offset:1024
	ds_read_b128 v[10:13], v198 offset:2048
	ds_read_b128 v[14:17], v198 offset:3072
	s_add_u32 s42, s46, 0x100
	s_addc_u32 s43, s47, 0
	s_add_u32 s48, s37, s46
	s_addc_u32 s49, s80, s47
	s_cmpk_eq_i32 s46, 0x300
	s_cselect_b64 vcc, -1, 0
	s_and_b64 s[44:45], vcc, exec
	s_cselect_b32 s81, 0, s42
	s_cselect_b32 s76, 0, s43
	s_cselect_b32 s44, s38, s48
	s_cselect_b32 s45, s39, s49
	s_add_u32 s48, s8, s81
	s_addc_u32 s49, s9, s76
	v_lshl_add_u64 v[228:229], v[180:181], 0, s[46:47]
	s_add_i32 m0, s41, 0xc000
	ds_read_b128 v[184:187], v199
	ds_read_b128 v[188:191], v199 offset:1024
	ds_read_b128 v[204:207], v199 offset:2048
	ds_read_b128 v[208:211], v199 offset:3072
	ds_read_b128 v[212:215], v199 offset:4096
	ds_read_b128 v[216:219], v199 offset:5120
	ds_read_b128 v[220:223], v199 offset:6144
	ds_read_b128 v[224:227], v199 offset:7168
	global_load_lds_dwordx4 v[228:229], off
	v_lshl_add_u64 v[228:229], v[182:183], 0, s[46:47]
	s_add_i32 m0, s41, 0xe000
	s_nop 0
	global_load_lds_dwordx4 v[228:229], off
	s_waitcnt vmcnt(8)
	s_waitcnt lgkmcnt(0)
	s_barrier
	s_setprio 1
	s_waitcnt lgkmcnt(0)
	v_mfma_scale_f32_16x16x128_f8f6f4 v[158:161], v[18:25], v[184:191], v[158:161], v163, v1 op_sel_hi:[0,0,0]
	v_mfma_scale_f32_16x16x128_f8f6f4 v[150:153], v[26:33], v[184:191], v[150:153], v163, v1 op_sel_hi:[0,0,0]
	v_mfma_scale_f32_16x16x128_f8f6f4 v[142:145], v[18:25], v[204:211], v[142:145], v163, v1 op_sel_hi:[0,0,0]
	v_mfma_scale_f32_16x16x128_f8f6f4 v[134:137], v[26:33], v[204:211], v[134:137], v163, v1 op_sel_hi:[0,0,0]
	v_mfma_scale_f32_16x16x128_f8f6f4 v[126:129], v[18:25], v[212:219], v[126:129], v163, v1 op_sel_hi:[0,0,0]
	v_mfma_scale_f32_16x16x128_f8f6f4 v[118:121], v[26:33], v[212:219], v[118:121], v163, v1 op_sel_hi:[0,0,0]
	v_mfma_scale_f32_16x16x128_f8f6f4 v[110:113], v[18:25], v[220:227], v[110:113], v163, v1 op_sel_hi:[0,0,0]
	v_mfma_scale_f32_16x16x128_f8f6f4 v[102:105], v[26:33], v[220:227], v[102:105], v163, v1 op_sel_hi:[0,0,0]
	s_setprio 0
	s_setprio 1
	v_mfma_scale_f32_16x16x128_f8f6f4 v[154:157], v[2:9], v[184:191], v[154:157], v163, v1 op_sel_hi:[0,0,0]
	v_mfma_scale_f32_16x16x128_f8f6f4 v[146:149], v[10:17], v[184:191], v[146:149], v163, v1 op_sel_hi:[0,0,0]
	v_mfma_scale_f32_16x16x128_f8f6f4 v[138:141], v[2:9], v[204:211], v[138:141], v163, v1 op_sel_hi:[0,0,0]
	v_mfma_scale_f32_16x16x128_f8f6f4 v[130:133], v[10:17], v[204:211], v[130:133], v163, v1 op_sel_hi:[0,0,0]
	v_mfma_scale_f32_16x16x128_f8f6f4 v[122:125], v[2:9], v[212:219], v[122:125], v163, v1 op_sel_hi:[0,0,0]
	v_mfma_scale_f32_16x16x128_f8f6f4 v[114:117], v[10:17], v[212:219], v[114:117], v163, v1 op_sel_hi:[0,0,0]
	v_mfma_scale_f32_16x16x128_f8f6f4 v[106:109], v[2:9], v[220:227], v[106:109], v163, v1 op_sel_hi:[0,0,0]
	v_mfma_scale_f32_16x16x128_f8f6f4 v[98:101], v[10:17], v[220:227], v[98:101], v163, v1 op_sel_hi:[0,0,0]
	s_setprio 0
	s_barrier
	s_add_i32 s46, s5, s52
	v_lshl_add_u64 v[184:185], s[44:45], 0, v[164:165]
	s_mov_b32 m0, s46
	ds_read_b128 v[204:207], v199 offset:16384
	ds_read_b128 v[208:211], v199 offset:17408
	ds_read_b128 v[212:215], v199 offset:18432
	ds_read_b128 v[216:219], v199 offset:19456
	ds_read_b128 v[220:223], v199 offset:20480
	ds_read_b128 v[224:227], v199 offset:21504
	ds_read_b128 v[228:231], v199 offset:22528
	ds_read_b128 v[232:235], v199 offset:23552
	global_load_lds_dwordx4 v[184:185], off
	s_add_i32 m0, s46, 0x2000
	s_add_u32 s46, s44, 0x20000
	v_lshl_add_u64 v[186:187], s[44:45], 0, v[166:167]
	s_addc_u32 s47, s45, 0
	s_add_i32 s76, s66, s52
	global_load_lds_dwordx4 v[186:187], off
	v_lshl_add_u64 v[188:189], s[46:47], 0, v[164:165]
	s_mov_b32 m0, s76
	v_cndmask_b32_e32 v168, v202, v179, vcc
	global_load_lds_dwordx4 v[188:189], off
	v_lshl_add_u64 v[188:189], s[46:47], 0, v[166:167]
	s_add_i32 m0, s76, 0x2000
	v_lshl_add_u64 v[190:191], s[48:49], 0, v[168:169]
	global_load_lds_dwordx4 v[188:189], off
	s_mov_b32 m0, s41
	v_cndmask_b32_e32 v188, v176, v201, vcc
	global_load_lds_dwordx4 v168, s[48:49]
	s_mov_b32 m0, s53
	v_mov_b32_e32 v189, v169
	global_load_lds_dwordx4 v188, s[48:49]
	s_waitcnt vmcnt(8)
	s_waitcnt lgkmcnt(0)
	v_lshl_or_b32 v179, v236, 10, v194
	v_lshl_or_b32 v175, v237, 10, v194
	v_lshl_or_b32 v201, v238, 10, v194
	v_lshl_or_b32 v200, v239, 10, v194
	v_lshl_add_u64 v[188:189], s[48:49], 0, v[188:189]
	s_barrier
	s_setprio 1
	s_waitcnt lgkmcnt(0)
	v_mfma_scale_f32_16x16x128_f8f6f4 v[94:97], v[18:25], v[204:211], v[94:97], v163, v1 op_sel_hi:[0,0,0]
	v_mfma_scale_f32_16x16x128_f8f6f4 v[86:89], v[26:33], v[204:211], v[86:89], v163, v1 op_sel_hi:[0,0,0]
	v_mfma_scale_f32_16x16x128_f8f6f4 v[78:81], v[18:25], v[212:219], v[78:81], v163, v1 op_sel_hi:[0,0,0]
	v_mfma_scale_f32_16x16x128_f8f6f4 v[70:73], v[26:33], v[212:219], v[70:73], v163, v1 op_sel_hi:[0,0,0]
	v_mfma_scale_f32_16x16x128_f8f6f4 v[58:61], v[18:25], v[220:227], v[58:61], v163, v1 op_sel_hi:[0,0,0]
	v_mfma_scale_f32_16x16x128_f8f6f4 v[46:49], v[26:33], v[220:227], v[46:49], v163, v1 op_sel_hi:[0,0,0]
	v_mfma_scale_f32_16x16x128_f8f6f4 v[38:41], v[18:25], v[228:235], v[38:41], v163, v1 op_sel_hi:[0,0,0]
	v_mfma_scale_f32_16x16x128_f8f6f4 v[34:37], v[26:33], v[228:235], v[34:37], v163, v1 op_sel_hi:[0,0,0]
	s_setprio 0
	s_setprio 1
	v_mfma_scale_f32_16x16x128_f8f6f4 v[90:93], v[2:9], v[204:211], v[90:93], v163, v1 op_sel_hi:[0,0,0]
	v_mfma_scale_f32_16x16x128_f8f6f4 v[82:85], v[10:17], v[204:211], v[82:85], v163, v1 op_sel_hi:[0,0,0]
	v_mfma_scale_f32_16x16x128_f8f6f4 v[74:77], v[2:9], v[212:219], v[74:77], v163, v1 op_sel_hi:[0,0,0]
	v_mfma_scale_f32_16x16x128_f8f6f4 v[66:69], v[10:17], v[212:219], v[66:69], v163, v1 op_sel_hi:[0,0,0]
	v_mfma_scale_f32_16x16x128_f8f6f4 v[50:53], v[2:9], v[220:227], v[50:53], v163, v1 op_sel_hi:[0,0,0]
	v_mfma_scale_f32_16x16x128_f8f6f4 v[42:45], v[10:17], v[220:227], v[42:45], v163, v1 op_sel_hi:[0,0,0]
	v_mfma_scale_f32_16x16x128_f8f6f4 v[62:65], v[2:9], v[228:235], v[62:65], v163, v1 op_sel_hi:[0,0,0]
	v_mfma_scale_f32_16x16x128_f8f6f4 v[54:57], v[10:17], v[228:235], v[54:57], v163, v1 op_sel_hi:[0,0,0]
	s_setprio 0
	s_barrier
	s_add_i32 s46, 0, 0x18000
	s_add_i32 s47, 0, 0x1c000
	v_add_u32_e32 v14, s46, v177
	v_add_u32_e32 v30, s47, v177
	ds_read_b128 v[2:5], v14
	ds_read_b128 v[6:9], v14 offset:1024
	ds_read_b128 v[10:13], v14 offset:2048
	ds_read_b128 v[14:17], v14 offset:3072
	ds_read_b128 v[18:21], v30
	ds_read_b128 v[22:25], v30 offset:1024
	ds_read_b128 v[26:29], v30 offset:2048
	ds_read_b128 v[30:33], v30 offset:3072
	s_mov_b32 m0, s59
	v_cndmask_b32_e32 v168, v174, v175, vcc
	ds_read_b128 v[204:207], v199 offset:32768
	ds_read_b128 v[208:211], v199 offset:33792
	ds_read_b128 v[212:215], v199 offset:34816
	ds_read_b128 v[216:219], v199 offset:35840
	ds_read_b128 v[220:223], v199 offset:36864
	ds_read_b128 v[224:227], v199 offset:37888
	ds_read_b128 v[228:231], v199 offset:38912
	ds_read_b128 v[232:235], v199 offset:39936
	v_cndmask_b32_e32 v170, v178, v200, vcc
	global_load_lds_dwordx4 v168, s[48:49]
	s_mov_b32 m0, s60
	s_nop 0
	global_load_lds_dwordx4 v170, s[48:49]
	s_waitcnt vmcnt(8)
	s_waitcnt lgkmcnt(0)
	s_barrier
	s_setprio 1
	s_waitcnt lgkmcnt(0)
	v_mfma_scale_f32_16x16x128_f8f6f4 v[158:161], v[2:9], v[204:211], v[158:161], v163, v1 op_sel_hi:[0,0,0]
	v_mfma_scale_f32_16x16x128_f8f6f4 v[150:153], v[10:17], v[204:211], v[150:153], v163, v1 op_sel_hi:[0,0,0]
	v_mfma_scale_f32_16x16x128_f8f6f4 v[142:145], v[2:9], v[212:219], v[142:145], v163, v1 op_sel_hi:[0,0,0]
	v_mfma_scale_f32_16x16x128_f8f6f4 v[134:137], v[10:17], v[212:219], v[134:137], v163, v1 op_sel_hi:[0,0,0]
	v_mfma_scale_f32_16x16x128_f8f6f4 v[126:129], v[2:9], v[220:227], v[126:129], v163, v1 op_sel_hi:[0,0,0]
	v_mfma_scale_f32_16x16x128_f8f6f4 v[118:121], v[10:17], v[220:227], v[118:121], v163, v1 op_sel_hi:[0,0,0]
	v_mfma_scale_f32_16x16x128_f8f6f4 v[110:113], v[2:9], v[228:235], v[110:113], v163, v1 op_sel_hi:[0,0,0]
	v_mfma_scale_f32_16x16x128_f8f6f4 v[102:105], v[10:17], v[228:235], v[102:105], v163, v1 op_sel_hi:[0,0,0]
	s_setprio 0
	s_setprio 1
	v_mfma_scale_f32_16x16x128_f8f6f4 v[154:157], v[18:25], v[204:211], v[154:157], v163, v1 op_sel_hi:[0,0,0]
	v_mfma_scale_f32_16x16x128_f8f6f4 v[146:149], v[26:33], v[204:211], v[146:149], v163, v1 op_sel_hi:[0,0,0]
	v_mfma_scale_f32_16x16x128_f8f6f4 v[138:141], v[18:25], v[212:219], v[138:141], v163, v1 op_sel_hi:[0,0,0]
	v_mfma_scale_f32_16x16x128_f8f6f4 v[130:133], v[26:33], v[212:219], v[130:133], v163, v1 op_sel_hi:[0,0,0]
	v_mfma_scale_f32_16x16x128_f8f6f4 v[122:125], v[18:25], v[220:227], v[122:125], v163, v1 op_sel_hi:[0,0,0]
	v_mfma_scale_f32_16x16x128_f8f6f4 v[114:117], v[26:33], v[220:227], v[114:117], v163, v1 op_sel_hi:[0,0,0]
	v_mfma_scale_f32_16x16x128_f8f6f4 v[106:109], v[18:25], v[228:235], v[106:109], v163, v1 op_sel_hi:[0,0,0]
	v_mfma_scale_f32_16x16x128_f8f6f4 v[98:101], v[26:33], v[228:235], v[98:101], v163, v1 op_sel_hi:[0,0,0]
	s_setprio 0
	s_barrier
	s_add_i32 s46, s46, s52
	v_lshl_add_u64 v[184:185], v[184:185], 0, s[16:17]
	s_mov_b32 m0, s46
	ds_read_b128 v[204:207], v199 offset:49152
	ds_read_b128 v[208:211], v199 offset:50176
	ds_read_b128 v[212:215], v199 offset:51200
	ds_read_b128 v[216:219], v199 offset:52224
	ds_read_b128 v[220:223], v199 offset:53248
	ds_read_b128 v[224:227], v199 offset:54272
	ds_read_b128 v[228:231], v199 offset:55296
	ds_read_b128 v[232:235], v199 offset:56320
	global_load_lds_dwordx4 v[184:185], off
	s_add_i32 m0, s46, 0x2000
	s_add_u32 s44, s44, 0x20080
	v_lshl_add_u64 v[184:185], v[186:187], 0, s[16:17]
	s_addc_u32 s45, s45, 0
	s_add_i32 s46, s47, s52
	global_load_lds_dwordx4 v[184:185], off
	v_lshl_add_u64 v[184:185], s[44:45], 0, v[164:165]
	s_mov_b32 m0, s46
	s_nop 0
	global_load_lds_dwordx4 v[184:185], off
	v_lshl_add_u64 v[184:185], s[44:45], 0, v[166:167]
	s_add_i32 m0, s46, 0x2000
	s_nop 0
	global_load_lds_dwordx4 v[184:185], off
	v_lshl_add_u64 v[184:185], v[190:191], 0, s[16:17]
	s_mov_b32 m0, s63
	s_nop 0
	global_load_lds_dwordx4 v[184:185], off
	v_lshl_add_u64 v[184:185], v[188:189], 0, s[16:17]
	s_mov_b32 m0, s64
	s_nop 0
	global_load_lds_dwordx4 v[184:185], off
	s_waitcnt vmcnt(8)
	s_waitcnt lgkmcnt(0)
	s_barrier
	s_setprio 1
	s_waitcnt lgkmcnt(0)
	v_mfma_scale_f32_16x16x128_f8f6f4 v[94:97], v[2:9], v[204:211], v[94:97], v163, v1 op_sel_hi:[0,0,0]
	v_mfma_scale_f32_16x16x128_f8f6f4 v[86:89], v[10:17], v[204:211], v[86:89], v163, v1 op_sel_hi:[0,0,0]
	v_mfma_scale_f32_16x16x128_f8f6f4 v[78:81], v[2:9], v[212:219], v[78:81], v163, v1 op_sel_hi:[0,0,0]
	v_mfma_scale_f32_16x16x128_f8f6f4 v[70:73], v[10:17], v[212:219], v[70:73], v163, v1 op_sel_hi:[0,0,0]
	v_mfma_scale_f32_16x16x128_f8f6f4 v[58:61], v[2:9], v[220:227], v[58:61], v163, v1 op_sel_hi:[0,0,0]
	v_mfma_scale_f32_16x16x128_f8f6f4 v[46:49], v[10:17], v[220:227], v[46:49], v163, v1 op_sel_hi:[0,0,0]
	v_mfma_scale_f32_16x16x128_f8f6f4 v[38:41], v[2:9], v[228:235], v[38:41], v163, v1 op_sel_hi:[0,0,0]
	v_mfma_scale_f32_16x16x128_f8f6f4 v[34:37], v[10:17], v[228:235], v[34:37], v163, v1 op_sel_hi:[0,0,0]
	s_setprio 0
	s_setprio 1
	v_mfma_scale_f32_16x16x128_f8f6f4 v[90:93], v[18:25], v[204:211], v[90:93], v163, v1 op_sel_hi:[0,0,0]
	v_mfma_scale_f32_16x16x128_f8f6f4 v[82:85], v[26:33], v[204:211], v[82:85], v163, v1 op_sel_hi:[0,0,0]
	v_mfma_scale_f32_16x16x128_f8f6f4 v[74:77], v[18:25], v[212:219], v[74:77], v163, v1 op_sel_hi:[0,0,0]
	v_mfma_scale_f32_16x16x128_f8f6f4 v[66:69], v[26:33], v[212:219], v[66:69], v163, v1 op_sel_hi:[0,0,0]
	v_mfma_scale_f32_16x16x128_f8f6f4 v[50:53], v[18:25], v[220:227], v[50:53], v163, v1 op_sel_hi:[0,0,0]
	v_mfma_scale_f32_16x16x128_f8f6f4 v[42:45], v[26:33], v[220:227], v[42:45], v163, v1 op_sel_hi:[0,0,0]
	v_mfma_scale_f32_16x16x128_f8f6f4 v[62:65], v[18:25], v[228:235], v[62:65], v163, v1 op_sel_hi:[0,0,0]
	v_mfma_scale_f32_16x16x128_f8f6f4 v[54:57], v[26:33], v[228:235], v[54:57], v163, v1 op_sel_hi:[0,0,0]
	s_setprio 0
	s_barrier
	s_add_i32 s79, s79, 2
	s_cmp_gt_u32 s79, 5
	s_mov_b64 s[46:47], s[42:43]
	s_cbranch_scc0 .LBB0_1911
	s_and_b64 vcc, exec, s[20:21]
	s_cbranch_vccz .LBB0_1914
	s_barrier
